# v27 + attention loop: nine K-tile and nine V-tile LDS addresses folded into ds_read offset immediates (18 v_add_u32 per iteration replaced by s_nop 0 wait-state placeholders)
# speedup vs baseline: 1.0004x; 1.0004x over previous
; #define LAS __attribute__((address_space(3)))
; __device__ __forceinline__ void convert_experts(Frame& F, int lo, int hi) {
;     ...
;     constexpr int NPAIRS = CONV_ITEMS / 2;
;     (void)lo; (void)hi;
; __device__ __forceinline__ void phase_attn(Frame& F) {
;     ...
;         const unsigned qrow = __umul24((unsigned)(128 * cu.n + ql), (unsigned)cu.d);
;         const float c1 = 0.125f * LOG2E;
;         const float nc2 = -__builtin_amdgcn_exp2f(-(float)(cu.h + 1)) * (float)cu.d * LOG2E;
;         const bool first = cu.n == 0;
;         f32x4 St[9];
;         const f32x4 eb = (f32x4){ef[0], ef[1], ef[2], ef[3]} * nc2;
;         float mx = -INFINITY;
;         bf16x8 kf[9][2];
; #pragma unroll
;         for (int T = 0; T < 9; ++T) { LAS unsigned char* ka = kb + (16 * (w + T) + fr) * ATT_ROWB + fq * 16; kf[T][0] = *(LAS bf16x8*)ka; kf[T][1] = *(LAS bf16x8*)(ka + 64); }
.Lcq_wd:
	v_mov_b64_e32 v[48:49], v[4:5]
	v_mov_b64_e32 v[46:47], v[2:3]
	v_mov_b64_e32 v[44:45], v[8:9]
	v_mov_b64_e32 v[42:43], v[6:7]
	s_lshl_b32 s65, 1, s35
	s_waitcnt lgkmcnt(0)
	s_barrier
	s_add_i32 s37, s30, 1
	v_cvt_f32_u32_e32 v54, s37
	v_cvt_f32_u32_e32 v55, s65
	v_add3_u32 v110, s85, v82, v90
	s_nop 0
	v_exp_f32_e64 v54, -v54
	s_nop 0
	s_nop 0
	s_nop 0
	v_mul_f32_e32 v79, v55, v54
	ds_read_b128 v[54:57], v110
	ds_read_b128 v[58:61], v110 offset:64
	ds_read_b128 v[62:65], v110 offset:2304
	ds_read_b128 v[66:69], v110 offset:2368
	ds_read_b128 v[70:73], v110 offset:4608
	ds_read_b128 v[74:77], v110 offset:4672
	ds_read_b128 v[112:115], v110 offset:6912
	ds_read_b128 v[116:119], v110 offset:6976
	s_nop 0
	ds_read_b128 v[120:123], v110 offset:9216
	ds_read_b128 v[124:127], v110 offset:9280
	s_nop 0
	ds_read_b128 v[128:131], v110 offset:11520
	ds_read_b128 v[132:135], v110 offset:11584
	s_nop 0
	ds_read_b128 v[136:139], v110 offset:13824
	ds_read_b128 v[140:143], v110 offset:13888
	s_nop 0
	s_nop 0
	ds_read_b128 v[144:147], v110 offset:16128
	ds_read_b128 v[148:151], v110 offset:16192
	ds_read_b128 v[152:155], v110 offset:18432
	ds_read_b128 v[156:159], v110 offset:18496
	s_sub_u32 s32, s32, 1
	s_cmp_lt_i32 s32, 0
	s_cbranch_scc0 .Lcq_cont_l
	s_mov_b32 s32, 3
	s_mov_b32 s95, 0
	s_cmp_eq_u32 s90, 0
	s_cbranch_scc1 .Lcq_none_l
	s_sub_u32 s90, s90, 1
	s_lshr_b32 s98, s89, 6
	s_and_b32 s99, s89, 63
	s_mul_hi_u32 s100, s98, 0xaaaaaaab
	s_lshr_b32 s100, s100, 1
	s_mul_i32 s101, s100, 3
	s_sub_u32 s101, s98, s101
	s_cmp_lt_u32 s100, 256
	s_cselect_b32 s98, 0, 3
	s_cselect_b32 s95, s100, 0
	s_add_u32 s98, s98, s101
	s_lshl_b32 s98, s98, 1
	v_readlane_b32 s96, v253, s98
	s_add_u32 s98, s98, 1
	v_readlane_b32 s97, v253, s98
	s_lshl_b32 s95, s95, 20
	s_nop 3
	s_add_u32 s96, s96, s95
	s_addc_u32 s97, s97, 0
	s_cmp_eq_u32 s101, 2
	s_cbranch_scc1 .Lcq_down_l
	s_lshr_b32 s95, s99, 3
	s_and_b32 s99, s99, 7
	s_lshl_b32 s98, s95, 17
	s_add_u32 s96, s96, s98
	s_addc_u32 s97, s97, 0
	s_lshl_b32 s98, s99, 7
	s_add_u32 s96, s96, s98
	s_addc_u32 s97, s97, 0
	s_lshl_b32 s100, s100, 19
	s_lshr_b32 s98, s99, 2
	s_lshl_b32 s98, s98, 18
	s_add_u32 s100, s100, s98
	s_and_b32 s98, s99, 3
	s_lshl_b32 s98, s98, 15
	s_add_u32 s100, s100, s98
	s_lshl_b32 s98, s101, 17
	s_add_u32 s100, s100, s98
	s_lshl_b32 s98, s95, 7
	s_add_u32 s100, s100, s98
	v_readlane_b32 s92, v253, 12
	v_readlane_b32 s93, v253, 13
	s_mov_b32 s94, 0xc3317218
	s_cmp_eq_u32 s101, 0
	s_cselect_b32 s94, 0xc2b8aa3b, s94
	s_nop 3
	s_add_u32 s92, s92, s100
	s_addc_u32 s93, s93, 0
	s_movk_i32 s95, 0x400
	s_movk_i32 s98, 0x400
	s_branch .Lcq_go_l

; #define LAS __attribute__((address_space(3)))
; __device__ __forceinline__ unsigned cvt_pk_bf16(float lo, float hi) { const f32x2_t v = {lo, hi}; return __builtin_bit_cast(unsigned, __builtin_convertvector(v, bf16x2_t)); }
; __device__ __forceinline__ void phase_attn(Frame& F) {
;     ...
;         for (int T = 0; T < 9; ++T) {
;             f32x4 sa = (f32x4){0.f, 0.f, 0.f, 0.f};
;             sa = __builtin_amdgcn_mfma_f32_16x16x32_bf16(kf[T][0], q0, sa, 0, 0, 0);
;             sa = __builtin_amdgcn_mfma_f32_16x16x32_bf16(kf[T][1], q1, sa, 0, 0, 0);
;             const float kT = (!first || w + T >= 8) ? nc2 * (float)(128 - 16 * T) : -INFINITY;
;             sa = sa * c1 + (eb + kT);
; #pragma unroll
;             for (int rg = 0; rg < 4; ++rg) {
;                 if (T == 0) sa[rg] = ef[rg] <= 0.f ? sa[rg] : -INFINITY;
;                 if (T == 8) sa[rg] = ef[rg] >= 0.f ? sa[rg] : -INFINITY;
;             }
;             St[T] = sa;
;             mx = fmaxf(mx, fmaxf(fmaxf(sa[0], sa[1]), fmaxf(sa[2], sa[3])));
;         }
;     ...
;         for (int T = 0; T < 9; ++T) {
;             u32x2 pw; pw.x = cvt_pk_bf16(St[T][0], St[T][1]); pw.y = cvt_pk_bf16(St[T][2], St[T][3]);
;             const s16x4 pb = __builtin_bit_cast(s16x4, pw);
;             LAS unsigned char* va = kb + ATT_VOFF + (16 * (w + T) + 4 * fq + (fr >> 2)) * ATT_ROWB + (8 * (fr & 3)) * 2;
.Lcq_none_l:
	s_cmp_lg_u32 s64, 0
	v_lshl_add_u32 v78, s64, 7, v86
	s_cselect_b64 s[64:65], -1, 0
	v_mul_f32_e32 v160, 0xbfb8aa3b, v79
	v_and_b32_e32 v110, 0xffffff, v78
	s_waitcnt lgkmcnt(14)
	v_mfma_f32_16x16x32_bf16 v[54:57], v[54:57], v[46:49], 0
	v_mul_f32_e32 v78, 0x43000000, v160
	s_or_b64 vcc, s[64:65], s[38:39]
	v_cndmask_b32_e32 v78, v109, v78, vcc
	v_mfma_f32_16x16x32_bf16 v[54:57], v[58:61], v[42:45], v[54:57]
	v_fma_f32 v162, v50, v160, v78
	v_fma_f32 v163, v51, v160, v78
	v_pk_fma_f32 v[78:79], v[52:53], v[160:161], v[78:79] op_sel_hi:[1,0,0]
	s_or_b64 vcc, s[64:65], s[40:41]
	s_nop 3
	v_pk_fma_f32 v[56:57], v[56:57], s[56:57], v[78:79] op_sel_hi:[1,0,1]
	v_pk_fma_f32 v[54:55], v[54:55], s[56:57], v[162:163] op_sel_hi:[1,0,1]
	v_cndmask_b32_e64 v164, v109, v56, s[10:11]
	v_cndmask_b32_e64 v162, v109, v54, s[6:7]
	v_cndmask_b32_e64 v163, v109, v55, s[8:9]
	v_cndmask_b32_e64 v165, v109, v57, s[12:13]
	v_mfma_f32_16x16x32_bf16 v[54:57], v[62:65], v[46:49], 0
	v_max_f32_e32 v58, v162, v163
	v_max_f32_e32 v59, v164, v165
	v_max3_f32 v62, v58, v59, s78
	v_mfma_f32_16x16x32_bf16 v[54:57], v[66:69], v[42:45], v[54:57]
	v_mul_f32_e32 v58, 0x42e00000, v160
	v_cndmask_b32_e32 v58, v109, v58, vcc
	v_pk_fma_f32 v[60:61], v[50:51], v[160:161], v[58:59] op_sel_hi:[1,0,0]
	v_pk_fma_f32 v[58:59], v[52:53], v[160:161], v[58:59] op_sel_hi:[1,0,0]
	s_or_b64 vcc, s[64:65], s[42:43]
	s_nop 2
	v_pk_fma_f32 v[166:167], v[56:57], s[56:57], v[58:59] op_sel_hi:[1,0,1]
	s_waitcnt lgkmcnt(13)
	v_mfma_f32_16x16x32_bf16 v[56:59], v[70:73], v[46:49], 0
	v_fma_f32 v78, v54, s56, v60
	v_fma_f32 v79, v55, s56, v61
	v_max_f32_e32 v54, v166, v167
	v_max3_f32 v63, v78, v79, v54
	s_waitcnt lgkmcnt(12)
	v_mfma_f32_16x16x32_bf16 v[54:57], v[74:77], v[42:45], v[56:59]
	s_nop 2
	v_mul_f32_e32 v58, 0x42c00000, v160
	v_cndmask_b32_e32 v58, v109, v58, vcc
	v_pk_fma_f32 v[60:61], v[50:51], v[160:161], v[58:59] op_sel_hi:[1,0,0]
	v_pk_fma_f32 v[58:59], v[52:53], v[160:161], v[58:59] op_sel_hi:[1,0,0]
	s_nop 0
	v_pk_fma_f32 v[76:77], v[54:55], s[56:57], v[60:61] op_sel_hi:[1,0,1]
	v_pk_fma_f32 v[74:75], v[56:57], s[56:57], v[58:59] op_sel_hi:[1,0,1]
	s_waitcnt lgkmcnt(11)
	v_mfma_f32_16x16x32_bf16 v[54:57], v[112:115], v[46:49], 0
	v_max_f32_e32 v58, v74, v75
	v_max3_f32 v58, v76, v77, v58
	v_max3_f32 v62, v62, v63, v58
	s_waitcnt lgkmcnt(10)
	v_mfma_f32_16x16x32_bf16 v[54:57], v[116:119], v[42:45], v[54:57]
	v_mul_f32_e32 v58, 0x42a00000, v160
	s_or_b64 vcc, s[64:65], s[44:45]
	v_cndmask_b32_e32 v58, v109, v58, vcc
	v_pk_fma_f32 v[60:61], v[50:51], v[160:161], v[58:59] op_sel_hi:[1,0,0]
	v_pk_fma_f32 v[58:59], v[52:53], v[160:161], v[58:59] op_sel_hi:[1,0,0]
	s_nop 2
	v_pk_fma_f32 v[72:73], v[54:55], s[56:57], v[60:61] op_sel_hi:[1,0,1]
	v_pk_fma_f32 v[70:71], v[56:57], s[56:57], v[58:59] op_sel_hi:[1,0,1]
	s_waitcnt lgkmcnt(9)
	v_mfma_f32_16x16x32_bf16 v[56:59], v[120:123], v[46:49], 0
	v_max_f32_e32 v54, v70, v71
	v_max3_f32 v63, v72, v73, v54
	s_or_b64 vcc, s[64:65], s[46:47]
	s_waitcnt lgkmcnt(8)
	v_mfma_f32_16x16x32_bf16 v[54:57], v[124:127], v[42:45], v[56:59]
	s_nop 2
	v_mul_f32_e32 v58, 0x42800000, v160
	v_cndmask_b32_e32 v58, v109, v58, vcc
	v_pk_fma_f32 v[60:61], v[50:51], v[160:161], v[58:59] op_sel_hi:[1,0,0]
	v_pk_fma_f32 v[58:59], v[52:53], v[160:161], v[58:59] op_sel_hi:[1,0,0]
	s_nop 0
	v_pk_fma_f32 v[68:69], v[54:55], s[56:57], v[60:61] op_sel_hi:[1,0,1]
	v_pk_fma_f32 v[66:67], v[56:57], s[56:57], v[58:59] op_sel_hi:[1,0,1]
	s_waitcnt lgkmcnt(7)
	v_mfma_f32_16x16x32_bf16 v[54:57], v[128:131], v[46:49], 0
	v_max_f32_e32 v58, v66, v67
	v_max3_f32 v58, v68, v69, v58
	v_max3_f32 v111, v62, v63, v58
	s_waitcnt lgkmcnt(6)
	v_mfma_f32_16x16x32_bf16 v[54:57], v[132:135], v[42:45], v[54:57]
	v_mul_f32_e32 v58, 0x42400000, v160
	s_or_b64 vcc, s[64:65], s[48:49]
	v_cndmask_b32_e32 v58, v109, v58, vcc
	v_pk_fma_f32 v[60:61], v[50:51], v[160:161], v[58:59] op_sel_hi:[1,0,0]
	v_pk_fma_f32 v[58:59], v[52:53], v[160:161], v[58:59] op_sel_hi:[1,0,0]
	s_nop 2
	v_pk_fma_f32 v[64:65], v[54:55], s[56:57], v[60:61] op_sel_hi:[1,0,1]
	v_pk_fma_f32 v[62:63], v[56:57], s[56:57], v[58:59] op_sel_hi:[1,0,1]
	s_waitcnt lgkmcnt(5)
	v_mfma_f32_16x16x32_bf16 v[56:59], v[136:139], v[46:49], 0
	v_max_f32_e32 v54, v62, v63
	v_max3_f32 v112, v64, v65, v54
	s_or_b64 vcc, s[64:65], s[50:51]
	s_waitcnt lgkmcnt(4)
	v_mfma_f32_16x16x32_bf16 v[54:57], v[140:143], v[42:45], v[56:59]
	s_nop 2
	v_mul_f32_e32 v58, 0x42000000, v160
	v_cndmask_b32_e32 v58, v109, v58, vcc
	v_pk_fma_f32 v[60:61], v[50:51], v[160:161], v[58:59] op_sel_hi:[1,0,0]
	v_pk_fma_f32 v[58:59], v[52:53], v[160:161], v[58:59] op_sel_hi:[1,0,0]
	s_nop 0
	v_pk_fma_f32 v[60:61], v[54:55], s[56:57], v[60:61] op_sel_hi:[1,0,1]
	v_pk_fma_f32 v[58:59], v[56:57], s[56:57], v[58:59] op_sel_hi:[1,0,1]
	s_waitcnt lgkmcnt(3)
	v_mfma_f32_16x16x32_bf16 v[54:57], v[144:147], v[46:49], 0
	v_max_f32_e32 v113, v58, v59
	v_max3_f32 v113, v60, v61, v113
	v_max3_f32 v111, v111, v112, v113
	s_waitcnt lgkmcnt(1)
	v_mfma_f32_16x16x32_bf16 v[46:49], v[152:155], v[46:49], 0
	s_or_b64 vcc, s[64:65], s[52:53]
	v_add3_u32 v144, s85, v89, v99
	s_nop 0
	v_mfma_f32_16x16x32_bf16 v[112:115], v[148:151], v[42:45], v[54:57]
	s_nop 0
	s_nop 0
	s_nop 0
	v_mul_f32_e32 v54, 0x41800000, v160
	s_waitcnt lgkmcnt(0)
; __device__ __forceinline__ void phase_attn(Frame& F) {
;     ...
;             LAS unsigned char* ob = F.lds + (buf ^ 1) * ABUF;
; #pragma unroll
;             for (int jj = 0; jj < 4; ++jj) { const int ch = tid + 512 * jj, row = ch >> 3, c16 = ch & 7;
;                 *(LAS u32x4*)(ob + row * ATT_ROWB + c16 * 16) = kr[jj]; *(LAS u32x4*)(ob + ATT_VOFF + row * ATT_ROWB + c16 * 16) = vr[jj]; }
;         }
;         const AttnUnit nu = un;
;         un = attn_decode(x8 * PER_X + (jl + 2 * G8 < jlast ? jl + 2 * G8 : jlast)); attn_issue(qkv, un, tid, kr, vr);
;         { const char* qb = (const char*)qkv + (((size_t)nu.b * SEQ + nu.r) * NPROJ + nu.h * 64) * 2; const unsigned qo = __umul24((unsigned)(128 * nu.n + ql), (unsigned)nu.d * (NPROJ * 2)) + 16u * fq;
;           qn0 = *(const bf16x8*)(qb + qo); qn1 = *(const bf16x8*)(qb + qo + 64); }
;         const unsigned qrow = __umul24((unsigned)(128 * cu.n + ql), (unsigned)cu.d);
;         const float c1 = 0.125f * LOG2E;
;         const float nc2 = -__builtin_amdgcn_exp2f(-(float)(cu.h + 1)) * (float)cu.d * LOG2E;
;         const bool first = cu.n == 0;
;         f32x4 St[9];
;         const f32x4 eb = (f32x4){ef[0], ef[1], ef[2], ef[3]} * nc2;
;         float mx = -INFINITY;
;         bf16x8 kf[9][2];
; #pragma unroll
;         for (int T = 0; T < 9; ++T) { LAS unsigned char* ka = kb + (16 * (w + T) + fr) * ATT_ROWB + fq * 16; kf[T][0] = *(LAS bf16x8*)ka; kf[T][1] = *(LAS bf16x8*)(ka + 64); }
;         __builtin_amdgcn_sched_barrier(0);
; #pragma unroll
;         for (int T = 0; T < 9; ++T) {
;             f32x4 sa = (f32x4){0.f, 0.f, 0.f, 0.f};
;             sa = __builtin_amdgcn_mfma_f32_16x16x32_bf16(kf[T][0], q0, sa, 0, 0, 0);
;             sa = __builtin_amdgcn_mfma_f32_16x16x32_bf16(kf[T][1], q1, sa, 0, 0, 0);
;             const float kT = (!first || w + T >= 8) ? nc2 * (float)(128 - 16 * T) : -INFINITY;
;             sa = sa * c1 + (eb + kT);
; #pragma unroll
;             for (int rg = 0; rg < 4; ++rg) {
;                 if (T == 0) sa[rg] = ef[rg] <= 0.f ? sa[rg] : -INFINITY;
;                 if (T == 8) sa[rg] = ef[rg] >= 0.f ? sa[rg] : -INFINITY;
;             }
;             St[T] = sa;
;             mx = fmaxf(mx, fmaxf(fmaxf(sa[0], sa[1]), fmaxf(sa[2], sa[3])));
;         }
;         mx = fmaxf(mx, __shfl_xor(mx, 16)); mx = fmaxf(mx, __shfl_xor(mx, 32));
;         f32x4 lv = (f32x4){0.f, 0.f, 0.f, 0.f};
	v_mfma_f32_16x16x32_bf16 v[42:45], v[156:159], v[42:45], v[46:49]
	s_add_i32 s37, s77, s70
	s_xor_b32 s79, s79, 1
	s_min_i32 s37, s37, s71
	s_mul_i32 s58, s79, 0x12000
	s_add_i32 s37, s37, s3
	v_add_u32_e32 v2, s58, v84
	s_mul_hi_i32 s58, s37, 0x2aaaaaab
	s_lshr_b32 s59, s58, 31
	s_ashr_i32 s58, s58, 4
	s_add_i32 s59, s58, s59
	s_mul_i32 s58, s59, 0x60
	s_sub_i32 s37, s37, s58
	s_ashr_i32 s58, s59, 3
	s_and_b32 s80, s59, 7
	v_add_u32_e32 v3, v2, v83
	s_cmp_gt_i32 s37, 31
	ds_write_b128 v3, v[38:41]
	ds_write_b128 v3, v[34:37] offset:36864
	v_add_u32_e32 v3, v2, v85
	s_cselect_b64 s[82:83], -1, 0
	s_cmp_gt_i32 s37, 63
	ds_write_b128 v3, v[30:33]
	ds_write_b128 v3, v[26:29] offset:36864
	v_add_u32_e32 v3, v2, v87
	v_add_u32_e32 v2, v2, v88
	s_cselect_b64 s[86:87], -1, 0
	ds_write_b128 v3, v[22:25]
	ds_write_b128 v3, v[18:21] offset:36864
	ds_write_b128 v2, v[14:17]
	ds_write_b128 v2, v[10:13] offset:36864
	v_cndmask_b32_e64 v2, 0, 1, s[86:87]
	s_cmp_lg_u64 s[82:83], 0
	v_readfirstlane_b32 s59, v2
	s_addc_u32 s81, s59, 0
	s_lshl_b32 s59, s81, 5
	s_lshl_b32 s82, s81, 1
	s_sub_i32 s37, s37, s59
	s_sub_i32 s59, 5, s82
	s_ashr_i32 s83, s37, s59
	s_lshl_b32 s59, -1, s59
	s_andn2_b32 s84, s37, s59
	s_ashr_i32 s59, s58, 31
	s_lshl_b64 s[86:87], s[58:59], 12
	s_ashr_i32 s37, s83, 31
	s_add_u32 s59, s86, s83
	s_addc_u32 s37, s87, s37
	s_mulk_i32 s37, 0xa00
	s_mul_hi_u32 s86, s59, 0xa00
	s_add_i32 s87, s86, s37
	s_mulk_i32 s59, 0xa00
	s_lshl_b32 s37, s80, 6
	s_or_b32 s86, s59, s37
	s_lshl_b64 s[86:87], s[86:87], 1
	s_add_u32 s37, s33, s86
	s_addc_u32 s59, s66, s87
	s_add_u32 s86, s37, 0x400
	s_addc_u32 s87, s59, 0
	s_lshl_b32 s59, s84, 7
	v_add_u32_e32 v2, s59, v81
	s_lshl_b32 s37, 0x1400, s82
	v_max_i32_e32 v3, 0, v2
	v_mul_u32_u24_e32 v3, s37, v3
	v_or_b32_e32 v3, v3, v80
	global_load_dwordx4 v[38:41], v3, s[86:87]
	global_load_dwordx4 v[34:37], v3, s[86:87] offset:1024
	v_max_i32_e32 v3, 0xffffffc0, v2
	v_add_u32_e32 v3, 64, v3
	v_mul_u32_u24_e32 v3, s37, v3
	v_or_b32_e32 v3, v3, v80
	global_load_dwordx4 v[30:33], v3, s[86:87]
	global_load_dwordx4 v[26:29], v3, s[86:87] offset:1024
	v_add_u32_e32 v3, s59, v1
	v_max_i32_e32 v2, 0xffffff40, v2
	v_max_i32_e32 v3, 0, v3
	v_add_u32_e32 v2, 0xc0, v2
	v_mul_u32_u24_e32 v3, s37, v3
	v_mul_u32_u24_e32 v2, s37, v2
	v_or_b32_e32 v3, v3, v80
	v_or_b32_e32 v2, v2, v80
	s_ashr_i32 s37, s36, 31
	global_load_dwordx4 v[22:25], v3, s[86:87]
	global_load_dwordx4 v[18:21], v3, s[86:87] offset:1024
	global_load_dwordx4 v[14:17], v2, s[86:87]
	global_load_dwordx4 v[10:13], v2, s[86:87] offset:1024
	s_lshl_b64 s[86:87], s[36:37], 12
	s_ashr_i32 s37, s73, 31
	s_add_u32 s59, s86, s73
	s_addc_u32 s37, s87, s37
	s_mulk_i32 s37, 0xa00
	s_mul_hi_u32 s86, s59, 0xa00
	s_add_i32 s87, s86, s37
	s_mulk_i32 s59, 0xa00
	s_lshl_b32 s37, s75, 6
	s_or_b32 s86, s59, s37
	s_lshl_b64 s[86:87], s[86:87], 1
	s_add_u32 s86, s33, s86
	s_addc_u32 s87, s66, s87
	s_lshl_b32 s37, 0x1400, s74
	v_lshl_add_u32 v2, s76, 7, v86
	s_and_b32 s37, s37, 0x555400
	v_mul_u32_u24_e32 v2, s37, v2
	v_or_b32_e32 v6, v2, v82
	global_load_dwordx4 v[2:5], v6, s[86:87]
	s_nop 0
	global_load_dwordx4 v[6:9], v6, s[86:87] offset:64
	v_cndmask_b32_e32 v54, v109, v54, vcc
	s_or_b64 vcc, s[64:65], s[54:55]
	v_pk_fma_f32 v[56:57], v[50:51], v[160:161], v[54:55] op_sel_hi:[1,0,0]
	v_mul_f32_e32 v46, 0, v160
	v_cndmask_b32_e32 v46, v109, v46, vcc
	v_pk_fma_f32 v[48:49], v[50:51], v[160:161], v[46:47] op_sel_hi:[1,0,0]
	v_pk_fma_f32 v[46:47], v[52:53], v[160:161], v[46:47] op_sel_hi:[1,0,0]
	v_pk_fma_f32 v[54:55], v[52:53], v[160:161], v[54:55] op_sel_hi:[1,0,0]
	v_pk_fma_f32 v[44:45], v[44:45], s[56:57], v[46:47] op_sel_hi:[1,0,1]
	v_pk_fma_f32 v[42:43], v[42:43], s[56:57], v[48:49] op_sel_hi:[1,0,1]
	v_cndmask_b32_e64 v48, v109, v44, s[18:19]
	v_and_b32_e32 v44, 64, v108
	v_pk_fma_f32 v[54:55], v[114:115], s[56:57], v[54:55] op_sel_hi:[1,0,1]
	v_cndmask_b32_e64 v47, v109, v43, s[16:17]
	v_cndmask_b32_e64 v49, v109, v45, s[20:21]
	v_xor_b32_e32 v43, 16, v108
	v_add_u32_e32 v44, 64, v44
	v_pk_fma_f32 v[56:57], v[112:113], s[56:57], v[56:57] op_sel_hi:[1,0,1]
	v_max_f32_e32 v112, v54, v55
	v_cndmask_b32_e64 v46, v109, v42, s[14:15]
	v_max_f32_e32 v42, v48, v49
	v_cmp_lt_i32_e32 vcc, v43, v44
	v_max3_f32 v112, v56, v57, v112
	v_max3_f32 v42, v46, v47, v42
	v_cndmask_b32_e32 v43, v108, v43, vcc
	v_max3_f32 v42, v111, v112, v42
	v_lshlrev_b32_e32 v142, 2, v43
	ds_bpermute_b32 v43, v142, v42
	s_waitcnt lgkmcnt(0)
	v_max_f32_e32 v43, v43, v43
	v_max_f32_e32 v42, v42, v43
	v_xor_b32_e32 v43, 32, v108
	v_cmp_lt_i32_e32 vcc, v43, v44
	s_nop 1
	v_cndmask_b32_e32 v43, v108, v43, vcc
	v_lshlrev_b32_e32 v143, 2, v43
	ds_bpermute_b32 v43, v143, v42
	s_waitcnt lgkmcnt(0)
	v_max_f32_e32 v43, v43, v43
	v_max_f32_e32 v111, v42, v43
	v_xor_b32_e32 v42, 0x80000000, v111
	v_mov_b32_e32 v43, v42
	v_mov_b32_e32 v44, v42
	v_mov_b32_e32 v45, v42
	ds_read_b64_tr_b16 v[120:121], v144 offset:36864
	v_pk_add_f32 v[118:119], v[166:167], v[44:45]
	v_pk_add_f32 v[112:113], v[164:165], v[44:45]
	v_exp_f32_e32 v126, v118
	v_exp_f32_e32 v127, v119
	ds_read_b64_tr_b16 v[118:119], v144 offset:36872
	v_pk_add_f32 v[114:115], v[162:163], v[42:43]
	v_exp_f32_e32 v112, v112
	v_exp_f32_e32 v114, v114
	v_exp_f32_e32 v113, v113
	v_exp_f32_e32 v115, v115
	ds_read_b64_tr_b16 v[128:129], v144 offset:36928
	ds_read_b64_tr_b16 v[130:131], v144 offset:36936
	v_pk_add_f32 v[134:135], v[76:77], v[42:43]
	v_cvt_pk_bf16_f32 v123, v112, v113
	v_cvt_pk_bf16_f32 v122, v114, v115
	v_pk_add_f32 v[116:117], v[112:113], 0 op_sel_hi:[1,0]
	v_pk_add_f32 v[124:125], v[114:115], 0 op_sel_hi:[1,0]
	s_waitcnt lgkmcnt(3)
; #define LAS __attribute__((address_space(3)))
; __device__ __forceinline__ unsigned cvt_pk_bf16(float lo, float hi) { const f32x2_t v = {lo, hi}; return __builtin_bit_cast(unsigned, __builtin_convertvector(v, bf16x2_t)); }
; __device__ __forceinline__ float fast_exp2(float x) { return __builtin_amdgcn_exp2f(x); }
; __device__ __forceinline__ s16x4 tr_read(LAS unsigned char* p) { return __builtin_bit_cast(s16x4, __builtin_amdgcn_ds_read_tr16_b64_v4i16((LAS s16x4*)p)); }
; __device__ __forceinline__ void phase_attn(Frame& F) {
;     ...
;         for (int T = 0; T < 9; ++T) { const f32x4 d = St[T] + nmx; f32x4 pv; pv.x = fast_exp2(d.x); pv.y = fast_exp2(d.y); pv.z = fast_exp2(d.z); pv.w = fast_exp2(d.w); St[T] = pv; lv = lv + pv; }
;         float l = (lv.x + lv.y) + (lv.z + lv.w);
;         l += __shfl_xor(l, 16); l += __shfl_xor(l, 32);
;         f32x4 O[4];
; #pragma unroll
;         for (int dt = 0; dt < 4; ++dt) O[dt] = (f32x4){0.f, 0.f, 0.f, 0.f};
; #pragma unroll
;         for (int T = 0; T < 9; ++T) {
;             u32x2 pw; pw.x = cvt_pk_bf16(St[T][0], St[T][1]); pw.y = cvt_pk_bf16(St[T][2], St[T][3]);
;             const s16x4 pb = __builtin_bit_cast(s16x4, pw);
;             LAS unsigned char* va = kb + ATT_VOFF + (16 * (w + T) + 4 * fq + (fr >> 2)) * ATT_ROWB + (8 * (fr & 3)) * 2;
; #pragma unroll
;             for (int dt = 0; dt < 4; ++dt) O[dt] = __builtin_amdgcn_mfma_f32_16x16x16bf16_1k(tr_read(va + 64 * (dt >> 1) + 8 * (dt & 1)), pb, O[dt], 0, 0, 0);
;         }
	v_mfma_f32_16x16x16_bf16 v[112:115], v[120:121], v[122:123], 0
	v_add_f32_e64 v120, v74, v44
	v_add_f32_e64 v121, v75, v45
	v_pk_add_f32 v[132:133], v[126:127], v[116:117]
	v_exp_f32_e32 v136, v120
	s_waitcnt lgkmcnt(2)
	v_mfma_f32_16x16x16_bf16 v[116:119], v[118:119], v[122:123], 0
	v_exp_f32_e32 v137, v121
	v_pk_add_f32 v[78:79], v[78:79], v[42:43]
	v_cvt_pk_bf16_f32 v139, v126, v127
	s_waitcnt lgkmcnt(1)
	v_mfma_f32_16x16x16_bf16 v[74:77], v[128:129], v[122:123], 0
	ds_read_b64_tr_b16 v[128:129], v144 offset:39168
	v_exp_f32_e32 v78, v78
	v_exp_f32_e32 v79, v79
	s_waitcnt lgkmcnt(1)
	v_mfma_f32_16x16x16_bf16 v[120:123], v[130:131], v[122:123], 0
	ds_read_b64_tr_b16 v[130:131], v144 offset:39176
	ds_read_b64_tr_b16 v[126:127], v144 offset:39232
	ds_read_b64_tr_b16 v[140:141], v144 offset:39240
	v_cvt_pk_bf16_f32 v138, v78, v79
	v_exp_f32_e32 v134, v134
	v_exp_f32_e32 v135, v135
	s_waitcnt lgkmcnt(3)
	v_mfma_f32_16x16x16_bf16 v[112:115], v[128:129], v[138:139], v[112:115]
	v_add_f32_e64 v128, v70, v44
	v_add_f32_e64 v129, v71, v45
	v_pk_add_f32 v[78:79], v[78:79], v[124:125]
	v_pk_add_f32 v[124:125], v[136:137], v[132:133]
	s_waitcnt lgkmcnt(2)
	v_mfma_f32_16x16x16_bf16 v[116:119], v[130:131], v[138:139], v[116:119]
	v_add_f32_e64 v130, v72, v42
	v_add_f32_e64 v131, v73, v43
	v_pk_add_f32 v[78:79], v[134:135], v[78:79]
	v_exp_f32_e32 v128, v128
	s_waitcnt lgkmcnt(1)
	v_mfma_f32_16x16x16_bf16 v[70:73], v[126:127], v[138:139], v[74:77]
	ds_read_b64_tr_b16 v[126:127], v144 offset:41472
	v_exp_f32_e32 v129, v129
	v_pk_add_f32 v[48:49], v[44:45], v[48:49]
	s_waitcnt lgkmcnt(1)
	v_mfma_f32_16x16x16_bf16 v[74:77], v[140:141], v[138:139], v[120:123]
	v_add_f32_e64 v124, v128, v124
	v_add_f32_e64 v125, v129, v125
	s_nop 0
	ds_read_b64_tr_b16 v[120:121], v144 offset:41480
	v_cvt_pk_bf16_f32 v122, v134, v135
	ds_read_b64_tr_b16 v[132:133], v144 offset:41536
	ds_read_b64_tr_b16 v[134:135], v144 offset:41544
	v_cvt_pk_bf16_f32 v123, v136, v137
	s_nop 0
	s_waitcnt lgkmcnt(3)
	v_mfma_f32_16x16x16_bf16 v[112:115], v[126:127], v[122:123], v[112:115]
	v_exp_f32_e32 v126, v130
	v_exp_f32_e32 v127, v131
	v_pk_add_f32 v[130:131], v[68:69], v[42:43]
	s_waitcnt lgkmcnt(2)
	v_mfma_f32_16x16x16_bf16 v[116:119], v[120:121], v[122:123], v[116:119]
	v_add_f32_e64 v120, v66, v44
	v_add_f32_e64 v121, v67, v45
	v_pk_add_f32 v[78:79], v[126:127], v[78:79]
	v_exp_f32_e32 v130, v130
	s_waitcnt lgkmcnt(1)
	v_mfma_f32_16x16x16_bf16 v[66:69], v[132:133], v[122:123], v[70:73]
	ds_read_b64_tr_b16 v[132:133], v144 offset:43776
	v_exp_f32_e32 v120, v120
	v_exp_f32_e32 v121, v121
	s_waitcnt lgkmcnt(1)
	v_mfma_f32_16x16x16_bf16 v[70:73], v[134:135], v[122:123], v[74:77]
	ds_read_b64_tr_b16 v[122:123], v144 offset:43784
	v_cvt_pk_bf16_f32 v134, v126, v127
	v_cvt_pk_bf16_f32 v135, v128, v129
	ds_read_b64_tr_b16 v[128:129], v144 offset:43840
	ds_read_b64_tr_b16 v[136:137], v144 offset:43848
	s_waitcnt lgkmcnt(3)
	v_mfma_f32_16x16x16_bf16 v[74:77], v[132:133], v[134:135], v[112:115]
	s_nop 0
	ds_read_b64_tr_b16 v[126:127], v144 offset:46088
	v_exp_f32_e32 v131, v131
	s_waitcnt lgkmcnt(3)
	v_mfma_f32_16x16x16_bf16 v[112:115], v[122:123], v[134:135], v[116:119]
	ds_read_b64_tr_b16 v[122:123], v144 offset:46080
	v_pk_add_f32 v[124:125], v[120:121], v[124:125]
	v_pk_add_f32 v[78:79], v[130:131], v[78:79]
	v_pk_add_f32 v[116:117], v[62:63], v[44:45]
	v_pk_add_f32 v[118:119], v[64:65], v[42:43]
	s_waitcnt lgkmcnt(3)
	v_mfma_f32_16x16x16_bf16 v[62:65], v[128:129], v[134:135], v[66:69]
	v_exp_f32_e32 v116, v116
	v_exp_f32_e32 v117, v117
	v_cvt_pk_bf16_f32 v128, v130, v131
	v_cvt_pk_bf16_f32 v129, v120, v121
	ds_read_b64_tr_b16 v[120:121], v144 offset:46144
	ds_read_b64_tr_b16 v[130:131], v144 offset:46152
	s_nop 0
	s_waitcnt lgkmcnt(4)
	v_mfma_f32_16x16x16_bf16 v[66:69], v[136:137], v[134:135], v[70:73]
	v_exp_f32_e32 v118, v118
	v_exp_f32_e32 v119, v119
	s_waitcnt lgkmcnt(2)
	v_mfma_f32_16x16x16_bf16 v[70:73], v[122:123], v[128:129], v[74:77]
	v_add_f32_e64 v122, v116, v124
	v_add_f32_e64 v123, v117, v125
	ds_read_b64_tr_b16 v[124:125], v144 offset:48392
	v_pk_add_f32 v[78:79], v[118:119], v[78:79]
	v_mfma_f32_16x16x16_bf16 v[74:77], v[126:127], v[128:129], v[112:115]
	v_cvt_pk_bf16_f32 v127, v116, v117
	v_cvt_pk_bf16_f32 v126, v118, v119
	s_nop 0
	v_pk_add_f32 v[112:113], v[58:59], v[44:45]
	v_pk_add_f32 v[114:115], v[60:61], v[42:43]
	s_waitcnt lgkmcnt(2)
	v_mfma_f32_16x16x16_bf16 v[58:61], v[120:121], v[128:129], v[62:65]
	ds_read_b64_tr_b16 v[120:121], v144 offset:48384
	v_exp_f32_e32 v112, v112
	v_exp_f32_e32 v113, v113
	v_exp_f32_e32 v114, v114
	s_waitcnt lgkmcnt(2)
	v_mfma_f32_16x16x16_bf16 v[62:65], v[130:131], v[128:129], v[66:69]
	ds_read_b64_tr_b16 v[116:117], v144 offset:48448
	ds_read_b64_tr_b16 v[128:129], v144 offset:48456
	v_exp_f32_e32 v115, v115
	v_pk_add_f32 v[118:119], v[112:113], v[122:123]
	s_nop 0
	s_waitcnt lgkmcnt(2)
	v_mfma_f32_16x16x16_bf16 v[66:69], v[120:121], v[126:127], v[70:73]
	ds_read_b64_tr_b16 v[120:121], v144 offset:50696
	v_mfma_f32_16x16x16_bf16 v[70:73], v[124:125], v[126:127], v[74:77]
	s_nop 2
	v_add_f32_e64 v74, v114, v78
	v_add_f32_e64 v75, v115, v79
	v_pk_add_f32 v[76:77], v[54:55], v[44:45]
	v_pk_add_f32 v[78:79], v[56:57], v[42:43]
	s_waitcnt lgkmcnt(2)
; #define LAS __attribute__((address_space(3)))
; __device__ __forceinline__ unsigned cvt_pk_bf16(float lo, float hi) { const f32x2_t v = {lo, hi}; return __builtin_bit_cast(unsigned, __builtin_convertvector(v, bf16x2_t)); }
; __device__ __forceinline__ s16x4 tr_read(LAS unsigned char* p) { return __builtin_bit_cast(s16x4, __builtin_amdgcn_ds_read_tr16_b64_v4i16((LAS s16x4*)p)); }
; __device__ __forceinline__ void phase_attn(Frame& F) {
;     ...
;         for (int T = 0; T < 9; ++T) {
;             u32x2 pw; pw.x = cvt_pk_bf16(St[T][0], St[T][1]); pw.y = cvt_pk_bf16(St[T][2], St[T][3]);
;             const s16x4 pb = __builtin_bit_cast(s16x4, pw);
;             LAS unsigned char* va = kb + ATT_VOFF + (16 * (w + T) + 4 * fq + (fr >> 2)) * ATT_ROWB + (8 * (fr & 3)) * 2;
; #pragma unroll
;             for (int dt = 0; dt < 4; ++dt) O[dt] = __builtin_amdgcn_mfma_f32_16x16x16bf16_1k(tr_read(va + 64 * (dt >> 1) + 8 * (dt & 1)), pb, O[dt], 0, 0, 0);
;         }
;         const float inv = 1.f / l;
;         bf16_t* op = (bf16_t*)((char*)part + (((size_t)cu.dsel * NTOK + (size_t)cu.b * SEQ + cu.r) * 512 + cu.h * 64) * 2 + (qrow * 1024u + 16u * fq));
; #pragma unroll
;         for (int u2 = 0; u2 < 2; ++u2) { u32x4 o4; o4.x = cvt_pk_bf16(O[2 * u2][0] * inv, O[2 * u2][1] * inv); o4.y = cvt_pk_bf16(O[2 * u2][2] * inv, O[2 * u2][3] * inv);
;             o4.z = cvt_pk_bf16(O[2 * u2 + 1][0] * inv, O[2 * u2 + 1][1] * inv); o4.w = cvt_pk_bf16(O[2 * u2 + 1][2] * inv, O[2 * u2 + 1][3] * inv); *(u32x4*)(op + 32 * u2) = o4; }
;         if (fq == 0) *(float*)((char*)lse + (((size_t)cu.dsel * NTOK + (size_t)cu.b * SEQ + cu.r) * 8 + cu.h) * 4 + qrow * 32u) = mx + __builtin_amdgcn_logf(l);
;         cu = nu; buf ^= 1;
	v_mfma_f32_16x16x16_bf16 v[54:57], v[116:117], v[126:127], v[58:61]
	ds_read_b64_tr_b16 v[116:117], v144 offset:50688
	v_cvt_pk_bf16_f32 v114, v114, v115
	v_cvt_pk_bf16_f32 v115, v112, v113
	ds_read_b64_tr_b16 v[112:113], v144 offset:50752
	ds_read_b64_tr_b16 v[122:123], v144 offset:50760
	s_waitcnt lgkmcnt(4)
	v_mfma_f32_16x16x16_bf16 v[58:61], v[128:129], v[126:127], v[62:65]
	v_exp_f32_e32 v76, v76
	v_exp_f32_e32 v77, v77
	v_exp_f32_e32 v78, v78
	s_waitcnt lgkmcnt(2)
	v_mfma_f32_16x16x16_bf16 v[62:65], v[116:117], v[114:115], v[66:69]
	v_exp_f32_e32 v79, v79
	v_pk_add_f32 v[116:117], v[76:77], v[118:119]
	v_mfma_f32_16x16x16_bf16 v[66:69], v[120:121], v[114:115], v[70:73]
	s_nop 2
	v_add_f32_e64 v70, v42, v46
	v_add_f32_e64 v71, v43, v47
	s_waitcnt lgkmcnt(1)
	v_mfma_f32_16x16x16_bf16 v[42:45], v[112:113], v[114:115], v[54:57]
	v_exp_f32_e32 v72, v48
	v_exp_f32_e32 v73, v49
	v_exp_f32_e32 v70, v70
	s_nop 0
	ds_read_b64_tr_b16 v[54:55], v144 offset:52992
	s_waitcnt lgkmcnt(1)
	v_mfma_f32_16x16x16_bf16 v[46:49], v[122:123], v[114:115], v[58:61]
	v_exp_f32_e32 v71, v71
	v_cvt_pk_bf16_f32 v112, v78, v79
	v_cvt_pk_bf16_f32 v113, v76, v77
	ds_read_b64_tr_b16 v[58:59], v144 offset:53000
	ds_read_b64_tr_b16 v[76:77], v144 offset:53056
	ds_read_b64_tr_b16 v[114:115], v144 offset:53064
	s_waitcnt lgkmcnt(3)
	v_mfma_f32_16x16x16_bf16 v[54:57], v[54:55], v[112:113], v[62:65]
	s_nop 2
	v_add_f32_e64 v62, v78, v74
	v_add_f32_e64 v63, v79, v75
	v_pk_add_f32 v[64:65], v[72:73], v[116:117]
	v_pk_add_f32 v[62:63], v[70:71], v[62:63]
	s_nop 0
	s_waitcnt lgkmcnt(2)
	v_mfma_f32_16x16x16_bf16 v[58:61], v[58:59], v[112:113], v[66:69]
	s_nop 2
	v_pk_mov_b32 v[66:67], v[62:63], v[64:65] op_sel:[1,0]
	v_mov_b32_e32 v63, v65
	ds_read_b64_tr_b16 v[64:65], v144 offset:55296
	v_pk_add_f32 v[62:63], v[66:67], v[62:63]
	v_cvt_pk_bf16_f32 v66, v70, v71
	v_add_f32_e32 v75, v62, v63
	v_cvt_pk_bf16_f32 v67, v72, v73
	s_waitcnt lgkmcnt(2)
	v_mfma_f32_16x16x16_bf16 v[42:45], v[76:77], v[112:113], v[42:45]
	ds_read_b64_tr_b16 v[62:63], v144 offset:55304
	ds_read_b64_tr_b16 v[68:69], v144 offset:55360
	ds_read_b64_tr_b16 v[70:71], v144 offset:55368
	s_waitcnt lgkmcnt(3)
	v_mfma_f32_16x16x16_bf16 v[54:57], v[64:65], v[66:67], v[54:57]
	ds_bpermute_b32 v64, v142, v75
	s_waitcnt lgkmcnt(0)
	v_add_f32_e32 v72, v75, v64
	ds_bpermute_b32 v73, v143, v72
	v_mfma_f32_16x16x16_bf16 v[58:61], v[62:63], v[66:67], v[58:61]
	v_mfma_f32_16x16x16_bf16 v[62:65], v[68:69], v[66:67], v[42:45]
	s_waitcnt lgkmcnt(0)
	s_nop 1
	v_add_f32_e32 v43, v72, v73
	v_div_scale_f32 v68, s[64:65], v43, v43, 1.0
	v_mfma_f32_16x16x16_bf16 v[46:49], v[114:115], v[112:113], v[46:49]
	v_rcp_f32_e32 v69, v68
	v_lshlrev_b32_e32 v42, s35, v110
	s_ashr_i32 s35, s34, 31
	v_mfma_f32_16x16x16_bf16 v[44:47], v[70:71], v[66:67], v[46:49]
	s_lshl_b64 s[64:65], s[26:27], 16
	s_lshl_b64 s[34:35], s[34:35], 12
	s_ashr_i32 s26, s31, 31
	s_nop 0
	v_fma_f32 v48, -v68, v69, 1.0
	v_fmac_f32_e32 v69, v48, v69
	v_div_scale_f32 v48, vcc, 1.0, v43, 1.0
	v_mul_f32_e32 v49, v48, v69
	s_add_u32 s31, s34, s31
	v_fma_f32 v66, -v68, v49, v48
	s_addc_u32 s26, s35, s26
	v_fmac_f32_e32 v49, v66, v69
	s_add_u32 s34, s31, s64
	v_fma_f32 v48, -v68, v49, v48
	s_addc_u32 s35, s26, s65
	v_div_fmas_f32 v48, v48, v69, v49
	s_lshl_b32 s26, s30, 7
	s_lshl_b64 s[64:65], s[34:35], 10
	v_div_fixup_f32 v48, v48, v43, 1.0
	s_add_u32 s31, s24, s64
	v_lshl_or_b32 v49, v42, 10, v82
	s_addc_u32 s37, s25, s65
	v_pk_mul_f32 v[54:55], v[48:49], v[54:55] op_sel_hi:[0,1]
	v_pk_mul_f32 v[56:57], v[48:49], v[56:57] op_sel_hi:[0,1]
	s_add_u32 s64, s31, s26
	v_cvt_pk_bf16_f32 v54, v54, v55
	v_cvt_pk_bf16_f32 v55, v56, v57
	v_pk_mul_f32 v[56:57], v[48:49], v[58:59] op_sel_hi:[0,1]
	v_pk_mul_f32 v[58:59], v[48:49], v[60:61] op_sel_hi:[0,1]
	s_addc_u32 s65, s37, 0
	v_cvt_pk_bf16_f32 v56, v56, v57
	v_cvt_pk_bf16_f32 v57, v58, v59
	global_store_dwordx4 v49, v[54:57], s[64:65]
	v_pk_mul_f32 v[44:45], v[48:49], v[44:45] op_sel_hi:[0,1]
	s_nop 0
	v_pk_mul_f32 v[54:55], v[48:49], v[62:63] op_sel_hi:[0,1]
	v_pk_mul_f32 v[56:57], v[48:49], v[64:65] op_sel_hi:[0,1]
	v_cvt_pk_bf16_f32 v54, v54, v55
	v_cvt_pk_bf16_f32 v55, v56, v57
	v_cvt_pk_bf16_f32 v56, v44, v45
	v_pk_mul_f32 v[44:45], v[48:49], v[46:47] op_sel_hi:[0,1]
	v_cvt_pk_bf16_f32 v57, v44, v45
	global_store_dwordx4 v49, v[54:57], s[64:65] offset:64
	s_cmp_eq_u32 s95, 0
	s_cbranch_scc1 .Lcq_skip_l
	s_waitcnt vmcnt(12)
	v_pk_mul_f32 v[168:169], v[168:169], s[94:95] op_sel_hi:[1,0]
	v_pk_mul_f32 v[170:171], v[170:171], s[94:95] op_sel_hi:[1,0]
	v_pk_mul_f32 v[172:173], v[172:173], s[94:95] op_sel_hi:[1,0]
	v_pk_mul_f32 v[174:175], v[174:175], s[94:95] op_sel_hi:[1,0]
	v_pk_mul_f32 v[176:177], v[176:177], s[94:95] op_sel_hi:[1,0]
	v_pk_mul_f32 v[178:179], v[178:179], s[94:95] op_sel_hi:[1,0]
	v_pk_mul_f32 v[180:181], v[180:181], s[94:95] op_sel_hi:[1,0]
	v_pk_mul_f32 v[182:183], v[182:183], s[94:95] op_sel_hi:[1,0]
	s_cmp_eq_u32 s32, 3
	s_cbranch_scc0 .Lcq_q1_l
	v_cvt_pk_fp8_f32 v232, v168, v172
	v_cvt_pk_fp8_f32 v236, v169, v173
	v_cvt_pk_fp8_f32 v240, v170, v174
	v_cvt_pk_fp8_f32 v244, v171, v175
	v_cvt_pk_fp8_f32 v232, v176, v180 op_sel:[0,0,1]
	v_cvt_pk_fp8_f32 v236, v177, v181 op_sel:[0,0,1]
	v_cvt_pk_fp8_f32 v240, v178, v182 op_sel:[0,0,1]
	v_cvt_pk_fp8_f32 v244, v179, v183 op_sel:[0,0,1]
	s_branch .Lcq_skip_l
